# baseline (speedup 1.0000x reference)
.LBB1_2:
	s_or_b64 exec, exec, s[8:9]
	s_ashr_i32 s9, s2, 3
	s_and_b32 s8, s2, 7
	s_and_b32 s9, s9, -8
	s_bfe_u32 s20, s3, 0x20006
	s_or_b32 s10, s9, s8
	s_lshl_b32 s2, s2, 4
	s_lshr_b32 s22, s3, 6
	v_bfe_u32 v1, v0, 5, 1
	s_and_b32 s2, s2, 0x380
	s_lshl_b32 s8, s20, 5
	s_ashr_i32 s11, s10, 31
	s_or_b32 s2, s8, s2
	s_lshl_b64 s[8:9], s[10:11], 19
	v_lshl_or_b32 v2, s22, 1, v1
	s_waitcnt lgkmcnt(0)
	s_cmpk_gt_u32 s3, 0xff
	s_cselect_b32 s44, s46, s44
	s_cselect_b32 s45, s47, s45
	v_and_b32_e32 v108, 0xff, v0
	v_lshlrev_b32_e32 v108, 2, v108
	global_load_dword v108, v108, s[44:45]
	s_add_u32 s14, s4, s8
	v_lshlrev_b32_e32 v6, 9, v2
	v_lshlrev_b32_e32 v2, 2, v2
	v_and_b32_e32 v5, 31, v0
	s_addc_u32 s15, s5, s9
	v_and_b32_e32 v2, 12, v2
	s_bfe_u32 s4, s3, 0x20007
	v_bitop3_b32 v2, v2, v5, s4 bitop3:0x36
	s_lshl_b32 s4, s22, 10
	v_lshl_or_b32 v192, v2, 4, v6
	s_add_i32 s21, s4, 0
	s_mov_b32 s4, m0
	s_mov_b32 m0, s21
	s_nop 0
	global_load_lds_dwordx4 v192, s[6:7]
	s_mov_b32 m0, s4
	s_add_u32 s4, s6, 0x2000
	s_addc_u32 s5, s7, 0
	s_add_i32 s31, s21, 0x2000
	s_mov_b32 s8, m0
	s_mov_b32 m0, s31
	s_nop 0
	global_load_lds_dwordx4 v192, s[4:5]
	s_mov_b32 m0, s8
	s_add_u32 s4, s6, 0x4000
	s_addc_u32 s5, s7, 0
	s_add_i32 s33, s21, 0x4000
	s_mov_b32 s8, m0
	s_mov_b32 m0, s33
	s_nop 0
	global_load_lds_dwordx4 v192, s[4:5]
	s_mov_b32 m0, s8
	s_add_u32 s4, s6, 0x6000
	s_addc_u32 s5, s7, 0
	s_add_i32 s34, s21, 0x6000
	s_mov_b32 s8, m0
	s_mov_b32 m0, s34
	s_nop 0
	global_load_lds_dwordx4 v192, s[4:5]
	s_mov_b32 m0, s8
	s_and_b32 s4, s2, 0x380
	s_lshl_b32 s4, s4, 9
	s_add_u32 s4, s14, s4
	s_addc_u32 s5, s15, 0
	s_add_i32 s27, s21, 0x10000
	s_add_i32 s28, s21, 0x12000
	s_add_i32 s29, s21, 0x14000
	s_add_i32 s30, s21, 0x16000
	s_mov_b32 s8, m0
	s_mov_b32 m0, s27
	s_nop 0
	global_load_lds_dwordx4 v192, s[4:5]
	s_mov_b32 m0, s8
	s_add_u32 s40, s4, 0x2000
	s_addc_u32 s41, s5, 0
	s_mov_b32 s8, m0
	s_mov_b32 m0, s28
	s_nop 0
	global_load_lds_dwordx4 v192, s[40:41]
	s_mov_b32 m0, s8
	s_add_u32 s40, s4, 0x4000
	s_addc_u32 s41, s5, 0
	s_mov_b32 s8, m0
	s_mov_b32 m0, s29
	s_nop 0
	global_load_lds_dwordx4 v192, s[40:41]
	s_mov_b32 m0, s8
	s_add_u32 s40, s4, 0x6000
	s_addc_u32 s41, s5, 0
	s_mov_b32 s8, m0
	s_mov_b32 m0, s30
	s_nop 0
	global_load_lds_dwordx4 v192, s[40:41]
	s_mov_b32 m0, s8
	s_add_u32 s40, s4, 0x8000
	s_addc_u32 s41, s5, 0
	s_add_i32 s42, s21, 0x18000
	s_mov_b32 s8, m0
	s_mov_b32 m0, s42
	s_nop 0
	global_load_lds_dwordx4 v192, s[40:41]
	s_mov_b32 m0, s8
	s_add_u32 s40, s4, 0xa000
	s_addc_u32 s41, s5, 0
	s_add_i32 s42, s21, 0x1a000
	s_mov_b32 s8, m0
	s_mov_b32 m0, s42
	s_nop 0
	global_load_lds_dwordx4 v192, s[40:41]
	s_mov_b32 m0, s8
	s_add_u32 s40, s4, 0xc000
	s_addc_u32 s41, s5, 0
	s_add_i32 s42, s21, 0x1c000
	s_mov_b32 s8, m0
	s_mov_b32 m0, s42
	s_nop 0
	global_load_lds_dwordx4 v192, s[40:41]
	s_mov_b32 m0, s8
	s_add_u32 s40, s4, 0xe000
	s_addc_u32 s41, s5, 0
	s_add_i32 s42, s21, 0x1e000
	s_mov_b32 s8, m0
	s_mov_b32 m0, s42
	s_nop 0
	global_load_lds_dwordx4 v192, s[40:41]
	s_mov_b32 m0, s8
	s_add_u32 s4, s6, 0x8000
	s_addc_u32 s5, s7, 0
	s_add_i32 s23, s21, 0x8000
	s_mov_b32 s8, m0
	s_mov_b32 m0, s23
	s_nop 0
	global_load_lds_dwordx4 v192, s[4:5]
	s_mov_b32 m0, s8
	s_add_u32 s4, s6, 0xa000
	s_addc_u32 s5, s7, 0
	s_add_i32 s24, s21, 0xa000
	s_mov_b32 s8, m0
	s_mov_b32 m0, s24
	s_nop 0
	global_load_lds_dwordx4 v192, s[4:5]
	s_mov_b32 m0, s8
	s_add_u32 s4, s6, 0xc000
	s_addc_u32 s5, s7, 0
	s_add_i32 s25, s21, 0xc000
	s_mov_b32 s8, m0
	s_mov_b32 m0, s25
	s_nop 0
	global_load_lds_dwordx4 v192, s[4:5]
	s_mov_b32 m0, s8
	s_add_u32 s4, s6, 0xe000
	s_addc_u32 s5, s7, 0
	s_add_i32 s26, s21, 0xe000
	s_mov_b32 s8, m0
	s_mov_b32 m0, s26
	s_nop 0
	global_load_lds_dwordx4 v192, s[4:5]
	s_mov_b32 m0, s8
	s_load_dwordx2 s[8:9], s[0:1], 0x18
	s_load_dwordx2 s[12:13], s[0:1], 0x28
	v_and_b32_e32 v81, 63, v0
	v_lshlrev_b32_e32 v2, 2, v0
	v_add_u32_e32 v6, 0x22000, v2
	s_waitcnt vmcnt(16)
	ds_write_b32 v6, v108
	s_lshr_b32 s5, s3, 8
	s_lshl_b32 s16, s20, 12
	s_lshl_b32 s4, s5, 5
	s_add_i32 s35, s16, 0
	s_add_u32 s18, s6, 0x18000
	v_and_b32_e32 v2, 12, v2
	v_bfe_u32 v0, v0, 2, 2
	s_addc_u32 s19, s7, 0
	v_bitop3_b32 v0, v2, v1, v0 bitop3:0x36
	s_add_u32 s16, s14, 0x8000
	v_lshlrev_b32_e32 v100, 4, v0
	v_or_b32_e32 v0, s4, v5
	s_addc_u32 s17, s15, 0
	s_lshl_b32 s36, s5, 7
	v_lshl_add_u32 v101, v0, 9, 0
	v_lshl_or_b32 v0, v1, 4, s36
	v_add_u32_e32 v0, 0, v0
	v_add_u32_e32 v83, v101, v100
	s_waitcnt vmcnt(4)
	s_waitcnt lgkmcnt(0)
	s_barrier
	s_lshl_b32 s40, s20, 14
	s_add_i32 s40, s40, 0x10000
	v_lshl_add_u32 v108, v5, 9, s40
	v_add_u32_e32 v109, v108, v100
	ds_read_b128 v[68:71], v109
	ds_read_b128 v[76:79], v109 offset:256
	v_xor_b32_e32 v109, 0x20, v100
	v_add_u32_e32 v109, v108, v109
	ds_read_b128 v[60:63], v109
	ds_read_b128 v[72:75], v109 offset:256
	v_xor_b32_e32 v109, 0x40, v100
	v_add_u32_e32 v109, v108, v109
	ds_read_b128 v[52:55], v109
	ds_read_b128 v[64:67], v109 offset:256
	v_xor_b32_e32 v109, 0x60, v100
	v_add_u32_e32 v109, v108, v109
	ds_read_b128 v[48:51], v109
	ds_read_b128 v[56:59], v109 offset:256
	v_xor_b32_e32 v109, 0x80, v100
	v_add_u32_e32 v109, v108, v109
	ds_read_b128 v[36:39], v109
	ds_read_b128 v[44:47], v109 offset:256
	v_xor_b32_e32 v109, 0xa0, v100
	v_add_u32_e32 v109, v108, v109
	ds_read_b128 v[28:31], v109
	ds_read_b128 v[40:43], v109 offset:256
	v_xor_b32_e32 v109, 0xc0, v100
	v_add_u32_e32 v109, v108, v109
	ds_read_b128 v[24:27], v109
	ds_read_b128 v[32:35], v109 offset:256
	v_xor_b32_e32 v109, 0xe0, v100
	v_add_u32_e32 v109, v108, v109
	ds_read_b128 v[20:23], v109
	ds_read_b128 v[16:19], v109 offset:256
	s_waitcnt vmcnt(0) lgkmcnt(0)
	s_barrier
	s_add_u32 s40, s6, 0x10000
	s_addc_u32 s41, s7, 0
	s_mov_b32 s42, m0
	s_mov_b32 m0, s27
	s_nop 0
	global_load_lds_dwordx4 v192, s[40:41]
	s_mov_b32 m0, s42
	s_add_u32 s40, s6, 0x12000
	s_addc_u32 s41, s7, 0
	s_mov_b32 s42, m0
	s_mov_b32 m0, s28
	s_nop 0
	global_load_lds_dwordx4 v192, s[40:41]
	s_mov_b32 m0, s42
	s_add_u32 s40, s6, 0x14000
	s_addc_u32 s41, s7, 0
	s_mov_b32 s42, m0
	s_mov_b32 m0, s29
	s_nop 0
	global_load_lds_dwordx4 v192, s[40:41]
	s_mov_b32 m0, s42
	s_add_u32 s40, s6, 0x16000
	s_addc_u32 s41, s7, 0
	s_mov_b32 s42, m0
	s_mov_b32 m0, s30
	s_nop 0
	global_load_lds_dwordx4 v192, s[40:41]
	s_mov_b32 m0, s42
	v_add_u32_e32 v80, 0x22000, v0
	v_lshl_add_u32 v81, v81, 4, s35
	v_add_u32_e32 v81, 0x18000, v81
	v_lshl_add_u32 v82, s5, 11, v81
	ds_read_b128 v[0:3], v80 offset:0
	ds_read_b128 v[4:7], v80 offset:32
	ds_read_b128 v[8:11], v80 offset:64
	ds_read_b128 v[12:15], v80 offset:96
	ds_read_b128 v[108:111], v80 offset:256
	ds_read_b128 v[112:115], v80 offset:288
	ds_read_b128 v[116:119], v80 offset:320
	ds_read_b128 v[120:123], v80 offset:352
	v_xor_b32_e32 v84, 0x20, v100
	v_add_u32_e32 v84, v101, v84
	v_xor_b32_e32 v85, 0x40, v100
	v_add_u32_e32 v85, v101, v85
	v_xor_b32_e32 v86, 0x60, v100
	v_add_u32_e32 v86, v101, v86
	v_xor_b32_e32 v87, 0x80, v100
	v_add_u32_e32 v87, v101, v87
	v_xor_b32_e32 v88, 0xa0, v100
	v_add_u32_e32 v88, v101, v88
	v_xor_b32_e32 v89, 0xc0, v100
	v_add_u32_e32 v89, v101, v89
	v_xor_b32_e32 v90, 0xe0, v100
	v_add_u32_e32 v90, v101, v90
	v_add_u32_e32 v208, 0x10000, v83
	v_add_u32_e32 v209, 0x10000, v84
	v_add_u32_e32 v210, 0x10000, v85
	v_add_u32_e32 v211, 0x10000, v86
	v_add_u32_e32 v212, 0x10000, v87
	v_add_u32_e32 v213, 0x10000, v88
	v_add_u32_e32 v214, 0x10000, v89
	v_add_u32_e32 v215, 0x10000, v90
	ds_read_b128 v[92:95], v83
	ds_read_b128 v[96:99], v83 offset:256
	ds_read_b128 v[200:203], v84
	ds_read_b128 v[204:207], v84 offset:256
	s_waitcnt lgkmcnt(8)
	s_waitcnt lgkmcnt(3)
	v_mfma_f32_32x32x16_bf16 v[0:15], v[92:95], v[68:71], v[0:15]
	s_waitcnt lgkmcnt(2)
	v_mfma_f32_32x32x16_bf16 v[0:15], v[96:99], v[76:79], v[0:15]
	ds_read_b128 v[92:95], v85
	ds_read_b128 v[96:99], v85 offset:256
	s_waitcnt lgkmcnt(3)
	v_mfma_f32_32x32x16_bf16 v[0:15], v[200:203], v[60:63], v[0:15]
	s_waitcnt lgkmcnt(2)
	v_mfma_f32_32x32x16_bf16 v[0:15], v[204:207], v[72:75], v[0:15]
	ds_read_b128 v[200:203], v86
	ds_read_b128 v[204:207], v86 offset:256
	s_waitcnt lgkmcnt(3)
	v_mfma_f32_32x32x16_bf16 v[0:15], v[92:95], v[52:55], v[0:15]
	s_waitcnt lgkmcnt(2)
	v_mfma_f32_32x32x16_bf16 v[0:15], v[96:99], v[64:67], v[0:15]
	ds_read_b128 v[92:95], v87
	ds_read_b128 v[96:99], v87 offset:256
	s_waitcnt lgkmcnt(3)
	v_mfma_f32_32x32x16_bf16 v[0:15], v[200:203], v[48:51], v[0:15]
	s_waitcnt lgkmcnt(2)
	v_mfma_f32_32x32x16_bf16 v[0:15], v[204:207], v[56:59], v[0:15]
	ds_read_b128 v[200:203], v88
	ds_read_b128 v[204:207], v88 offset:256
	s_waitcnt lgkmcnt(3)
	v_mfma_f32_32x32x16_bf16 v[0:15], v[92:95], v[36:39], v[0:15]
	s_waitcnt lgkmcnt(2)
	v_mfma_f32_32x32x16_bf16 v[0:15], v[96:99], v[44:47], v[0:15]
	ds_read_b128 v[92:95], v89
	ds_read_b128 v[96:99], v89 offset:256
	s_waitcnt lgkmcnt(3)
	v_mfma_f32_32x32x16_bf16 v[0:15], v[200:203], v[28:31], v[0:15]
	s_waitcnt lgkmcnt(2)
	v_mfma_f32_32x32x16_bf16 v[0:15], v[204:207], v[40:43], v[0:15]
	ds_read_b128 v[200:203], v90
	ds_read_b128 v[204:207], v90 offset:256
	s_waitcnt lgkmcnt(3)
	v_mfma_f32_32x32x16_bf16 v[0:15], v[92:95], v[24:27], v[0:15]
	s_waitcnt lgkmcnt(2)
	v_mfma_f32_32x32x16_bf16 v[0:15], v[96:99], v[32:35], v[0:15]
	ds_read_b128 v[92:95], v83 offset:32768
	ds_read_b128 v[96:99], v83 offset:33024
	s_waitcnt lgkmcnt(3)
	v_mfma_f32_32x32x16_bf16 v[0:15], v[200:203], v[20:23], v[0:15]
	s_waitcnt lgkmcnt(2)
	v_mfma_f32_32x32x16_bf16 v[0:15], v[204:207], v[16:19], v[0:15]
	ds_read_b128 v[200:203], v84 offset:32768
	ds_read_b128 v[204:207], v84 offset:33024
	s_waitcnt lgkmcnt(15)
	s_waitcnt lgkmcnt(3)
	v_mfma_f32_32x32x16_bf16 v[108:123], v[92:95], v[68:71], v[108:123]
	s_waitcnt lgkmcnt(2)
	v_mfma_f32_32x32x16_bf16 v[108:123], v[96:99], v[76:79], v[108:123]
	ds_read_b128 v[92:95], v85 offset:32768
	ds_read_b128 v[96:99], v85 offset:33024
	s_waitcnt lgkmcnt(3)
	v_mfma_f32_32x32x16_bf16 v[108:123], v[200:203], v[60:63], v[108:123]
	s_waitcnt lgkmcnt(2)
	v_mfma_f32_32x32x16_bf16 v[108:123], v[204:207], v[72:75], v[108:123]
	ds_read_b128 v[200:203], v86 offset:32768
	ds_read_b128 v[204:207], v86 offset:33024
	s_nop 1
	v_cvt_pk_bf16_f32 v216, v0, v1
	v_cvt_pk_bf16_f32 v217, v2, v3
	v_cvt_pk_bf16_f32 v218, v4, v5
	v_cvt_pk_bf16_f32 v219, v6, v7
	v_cvt_pk_bf16_f32 v220, v8, v9
	v_cvt_pk_bf16_f32 v221, v10, v11
	v_cvt_pk_bf16_f32 v222, v12, v13
	v_cvt_pk_bf16_f32 v223, v14, v15
	ds_write_b128 v82, v[216:219]
	ds_write_b128 v82, v[220:223] offset:1024
	s_waitcnt lgkmcnt(5)
	v_mfma_f32_32x32x16_bf16 v[108:123], v[92:95], v[52:55], v[108:123]
	s_waitcnt lgkmcnt(4)
	v_mfma_f32_32x32x16_bf16 v[108:123], v[96:99], v[64:67], v[108:123]
	ds_read_b128 v[92:95], v87 offset:32768
	ds_read_b128 v[96:99], v87 offset:33024
	s_waitcnt vmcnt(0)
	s_waitcnt lgkmcnt(2)
	s_barrier
	s_add_u32 s40, s6, 0x18000
	s_addc_u32 s41, s7, 0
	s_mov_b32 s42, m0
	s_mov_b32 m0, s21
	s_nop 0
	global_load_lds_dwordx4 v192, s[40:41]
	s_mov_b32 m0, s42
	s_add_u32 s40, s6, 0x1a000
	s_addc_u32 s41, s7, 0
	s_mov_b32 s42, m0
	s_mov_b32 m0, s31
	s_nop 0
	global_load_lds_dwordx4 v192, s[40:41]
	s_mov_b32 m0, s42
	s_waitcnt lgkmcnt(5)
	v_mfma_f32_32x32x16_bf16 v[108:123], v[200:203], v[48:51], v[108:123]
	s_waitcnt lgkmcnt(4)
	v_mfma_f32_32x32x16_bf16 v[108:123], v[204:207], v[56:59], v[108:123]
	ds_read_b128 v[200:203], v88 offset:32768
	ds_read_b128 v[204:207], v88 offset:33024
	s_add_u32 s40, s6, 0x1c000
	s_addc_u32 s41, s7, 0
	s_mov_b32 s42, m0
	s_mov_b32 m0, s33
	s_nop 0
	global_load_lds_dwordx4 v192, s[40:41]
	s_mov_b32 m0, s42
	s_add_u32 s40, s6, 0x1e000
	s_addc_u32 s41, s7, 0
	s_mov_b32 s42, m0
	s_mov_b32 m0, s34
	s_nop 0
	global_load_lds_dwordx4 v192, s[40:41]
	s_mov_b32 m0, s42
	ds_read_b128 v[128:131], v81
	ds_read_b128 v[132:135], v81 offset:1024
	ds_read_b128 v[136:139], v81 offset:2048
	ds_read_b128 v[140:143], v81 offset:3072
	ds_read_b128 v[0:3], v80 offset:512
	ds_read_b128 v[4:7], v80 offset:544
	ds_read_b128 v[8:11], v80 offset:576
	ds_read_b128 v[12:15], v80 offset:608
	s_waitcnt lgkmcnt(11)
	v_mfma_f32_32x32x16_bf16 v[108:123], v[92:95], v[36:39], v[108:123]
	s_waitcnt lgkmcnt(10)
	v_mfma_f32_32x32x16_bf16 v[108:123], v[96:99], v[44:47], v[108:123]
	ds_read_b128 v[92:95], v89 offset:32768
	ds_read_b128 v[96:99], v89 offset:33024
	s_waitcnt lgkmcnt(11)
	v_mfma_f32_32x32x16_bf16 v[108:123], v[200:203], v[28:31], v[108:123]
	s_waitcnt lgkmcnt(10)
	v_mfma_f32_32x32x16_bf16 v[108:123], v[204:207], v[40:43], v[108:123]
	ds_read_b128 v[200:203], v90 offset:32768
	ds_read_b128 v[204:207], v90 offset:33024
	s_waitcnt lgkmcnt(3)
	v_mfma_f32_32x32x16_bf16 v[108:123], v[92:95], v[24:27], v[108:123]
	s_waitcnt lgkmcnt(2)
	v_mfma_f32_32x32x16_bf16 v[108:123], v[96:99], v[32:35], v[108:123]
	ds_read_b128 v[92:95], v208
	ds_read_b128 v[96:99], v208 offset:256
	s_waitcnt lgkmcnt(3)
	v_mfma_f32_32x32x16_bf16 v[108:123], v[200:203], v[20:23], v[108:123]
	s_waitcnt lgkmcnt(2)
	v_mfma_f32_32x32x16_bf16 v[108:123], v[204:207], v[16:19], v[108:123]
	ds_read_b128 v[200:203], v209
	ds_read_b128 v[204:207], v209 offset:256
	s_waitcnt lgkmcnt(8)
	s_waitcnt lgkmcnt(3)
	v_mfma_f32_32x32x16_bf16 v[0:15], v[92:95], v[68:71], v[0:15]
	s_waitcnt lgkmcnt(2)
	v_mfma_f32_32x32x16_bf16 v[0:15], v[96:99], v[76:79], v[0:15]
	ds_read_b128 v[92:95], v210
	ds_read_b128 v[96:99], v210 offset:256
	s_waitcnt lgkmcnt(3)
	v_mfma_f32_32x32x16_bf16 v[0:15], v[200:203], v[60:63], v[0:15]
	s_waitcnt lgkmcnt(2)
	v_mfma_f32_32x32x16_bf16 v[0:15], v[204:207], v[72:75], v[0:15]
	ds_read_b128 v[200:203], v211
	ds_read_b128 v[204:207], v211 offset:256
	s_nop 1
	v_cvt_pk_bf16_f32 v216, v108, v109
	v_cvt_pk_bf16_f32 v217, v110, v111
	v_cvt_pk_bf16_f32 v218, v112, v113
	v_cvt_pk_bf16_f32 v219, v114, v115
	v_cvt_pk_bf16_f32 v220, v116, v117
	v_cvt_pk_bf16_f32 v221, v118, v119
	v_cvt_pk_bf16_f32 v222, v120, v121
	v_cvt_pk_bf16_f32 v223, v122, v123
	ds_write_b128 v82, v[216:219] offset:20480
	ds_write_b128 v82, v[220:223] offset:21504
	s_waitcnt lgkmcnt(5)
	v_mfma_f32_32x32x16_bf16 v[0:15], v[92:95], v[52:55], v[0:15]
	s_waitcnt lgkmcnt(4)
	v_mfma_f32_32x32x16_bf16 v[0:15], v[96:99], v[64:67], v[0:15]
	ds_read_b128 v[92:95], v212
	ds_read_b128 v[96:99], v212 offset:256
	s_waitcnt lgkmcnt(5)
	v_mfma_f32_32x32x16_bf16 v[0:15], v[200:203], v[48:51], v[0:15]
	s_waitcnt lgkmcnt(4)
	v_mfma_f32_32x32x16_bf16 v[0:15], v[204:207], v[56:59], v[0:15]
	ds_read_b128 v[200:203], v213
	ds_read_b128 v[204:207], v213 offset:256
	ds_read_b128 v[108:111], v80 offset:768
	ds_read_b128 v[112:115], v80 offset:800
	ds_read_b128 v[116:119], v80 offset:832
	ds_read_b128 v[120:123], v80 offset:864
	s_waitcnt lgkmcnt(7)
	v_mfma_f32_32x32x16_bf16 v[0:15], v[92:95], v[36:39], v[0:15]
	s_waitcnt lgkmcnt(6)
	v_mfma_f32_32x32x16_bf16 v[0:15], v[96:99], v[44:47], v[0:15]
	ds_read_b128 v[92:95], v214
	ds_read_b128 v[96:99], v214 offset:256
	s_waitcnt lgkmcnt(7)
	v_mfma_f32_32x32x16_bf16 v[0:15], v[200:203], v[28:31], v[0:15]
	s_waitcnt lgkmcnt(6)
	v_mfma_f32_32x32x16_bf16 v[0:15], v[204:207], v[40:43], v[0:15]
	ds_read_b128 v[200:203], v215
	ds_read_b128 v[204:207], v215 offset:256
	s_waitcnt vmcnt(0)
	s_waitcnt lgkmcnt(12)
	s_barrier
	s_add_u32 s40, s14, 0x0
	s_addc_u32 s41, s15, 0
	s_mov_b32 s42, m0
	s_mov_b32 m0, s23
	s_nop 0
	global_load_lds_dwordx4 v192, s[40:41]
	s_mov_b32 m0, s42
	s_add_u32 s40, s14, 0x2000
	s_addc_u32 s41, s15, 0
	s_mov_b32 s42, m0
	s_mov_b32 m0, s24
	s_nop 0
	global_load_lds_dwordx4 v192, s[40:41]
	s_mov_b32 m0, s42
	s_waitcnt lgkmcnt(3)
	v_mfma_f32_32x32x16_bf16 v[0:15], v[92:95], v[24:27], v[0:15]
	s_waitcnt lgkmcnt(2)
	v_mfma_f32_32x32x16_bf16 v[0:15], v[96:99], v[32:35], v[0:15]
	ds_read_b128 v[92:95], v83
	ds_read_b128 v[96:99], v83 offset:256
	s_add_u32 s40, s14, 0x4000
	s_addc_u32 s41, s15, 0
	s_mov_b32 s42, m0
	s_mov_b32 m0, s25
	s_nop 0
	global_load_lds_dwordx4 v192, s[40:41]
	s_mov_b32 m0, s42
	s_add_u32 s40, s14, 0x6000
	s_addc_u32 s41, s15, 0
	s_mov_b32 s42, m0
	s_mov_b32 m0, s26
	s_nop 0
	global_load_lds_dwordx4 v192, s[40:41]
	s_mov_b32 m0, s42
	ds_read_b128 v[144:147], v81 offset:20480
	ds_read_b128 v[148:151], v81 offset:21504
	ds_read_b128 v[152:155], v81 offset:22528
	ds_read_b128 v[156:159], v81 offset:23552
	s_waitcnt lgkmcnt(7)
	v_mfma_f32_32x32x16_bf16 v[0:15], v[200:203], v[20:23], v[0:15]
	s_waitcnt lgkmcnt(6)
	v_mfma_f32_32x32x16_bf16 v[0:15], v[204:207], v[16:19], v[0:15]
	ds_read_b128 v[200:203], v84
	ds_read_b128 v[204:207], v84 offset:256
	s_waitcnt lgkmcnt(12)
	s_waitcnt lgkmcnt(7)
	v_mfma_f32_32x32x16_bf16 v[108:123], v[92:95], v[68:71], v[108:123]
	s_waitcnt lgkmcnt(6)
	v_mfma_f32_32x32x16_bf16 v[108:123], v[96:99], v[76:79], v[108:123]
	ds_read_b128 v[92:95], v85
	ds_read_b128 v[96:99], v85 offset:256
	s_waitcnt lgkmcnt(3)
	v_mfma_f32_32x32x16_bf16 v[108:123], v[200:203], v[60:63], v[108:123]
	s_waitcnt lgkmcnt(2)
	v_mfma_f32_32x32x16_bf16 v[108:123], v[204:207], v[72:75], v[108:123]
	ds_read_b128 v[200:203], v86
	ds_read_b128 v[204:207], v86 offset:256
	s_nop 1
	v_cvt_pk_bf16_f32 v216, v0, v1
	v_cvt_pk_bf16_f32 v217, v2, v3
	v_cvt_pk_bf16_f32 v218, v4, v5
	v_cvt_pk_bf16_f32 v219, v6, v7
	v_cvt_pk_bf16_f32 v220, v8, v9
	v_cvt_pk_bf16_f32 v221, v10, v11
	v_cvt_pk_bf16_f32 v222, v12, v13
	v_cvt_pk_bf16_f32 v223, v14, v15
	ds_write_b128 v82, v[216:219]
	ds_write_b128 v82, v[220:223] offset:1024
	s_waitcnt lgkmcnt(5)
	v_mfma_f32_32x32x16_bf16 v[108:123], v[92:95], v[52:55], v[108:123]
	s_waitcnt lgkmcnt(4)
	v_mfma_f32_32x32x16_bf16 v[108:123], v[96:99], v[64:67], v[108:123]
	ds_read_b128 v[92:95], v87
	ds_read_b128 v[96:99], v87 offset:256
	s_waitcnt lgkmcnt(5)
	v_mfma_f32_32x32x16_bf16 v[108:123], v[200:203], v[48:51], v[108:123]
	s_waitcnt lgkmcnt(4)
	v_mfma_f32_32x32x16_bf16 v[108:123], v[204:207], v[56:59], v[108:123]
	ds_read_b128 v[200:203], v88
	ds_read_b128 v[204:207], v88 offset:256
	s_waitcnt lgkmcnt(4)
	s_barrier
	s_add_u32 s40, s14, 0x8000
	s_addc_u32 s41, s15, 0
	s_mov_b32 s42, m0
	s_mov_b32 m0, s27
	s_nop 0
	global_load_lds_dwordx4 v192, s[40:41]
	s_mov_b32 m0, s42
	s_add_u32 s40, s14, 0xa000
	s_addc_u32 s41, s15, 0
	s_mov_b32 s42, m0
	s_mov_b32 m0, s28
	s_nop 0
	global_load_lds_dwordx4 v192, s[40:41]
	s_mov_b32 m0, s42
	s_waitcnt lgkmcnt(3)
	v_mfma_f32_32x32x16_bf16 v[108:123], v[92:95], v[36:39], v[108:123]
	s_waitcnt lgkmcnt(2)
	v_mfma_f32_32x32x16_bf16 v[108:123], v[96:99], v[44:47], v[108:123]
	ds_read_b128 v[92:95], v89
	ds_read_b128 v[96:99], v89 offset:256
	s_add_u32 s40, s14, 0xc000
	s_addc_u32 s41, s15, 0
	s_mov_b32 s42, m0
	s_mov_b32 m0, s29
	s_nop 0
	global_load_lds_dwordx4 v192, s[40:41]
	s_mov_b32 m0, s42
	s_add_u32 s40, s14, 0xe000
	s_addc_u32 s41, s15, 0
	s_mov_b32 s42, m0
	s_mov_b32 m0, s30
	s_nop 0
	global_load_lds_dwordx4 v192, s[40:41]
	s_mov_b32 m0, s42
	ds_read_b128 v[160:163], v81
	ds_read_b128 v[164:167], v81 offset:1024
	ds_read_b128 v[168:171], v81 offset:2048
	ds_read_b128 v[172:175], v81 offset:3072
	s_waitcnt lgkmcnt(7)
	v_mfma_f32_32x32x16_bf16 v[108:123], v[200:203], v[28:31], v[108:123]
	s_waitcnt lgkmcnt(6)
	v_mfma_f32_32x32x16_bf16 v[108:123], v[204:207], v[40:43], v[108:123]
	ds_read_b128 v[200:203], v90
	ds_read_b128 v[204:207], v90 offset:256
	s_waitcnt lgkmcnt(7)
	v_mfma_f32_32x32x16_bf16 v[108:123], v[92:95], v[24:27], v[108:123]
	s_waitcnt lgkmcnt(6)
	v_mfma_f32_32x32x16_bf16 v[108:123], v[96:99], v[32:35], v[108:123]
	s_waitcnt lgkmcnt(1)
	v_mfma_f32_32x32x16_bf16 v[108:123], v[200:203], v[20:23], v[108:123]
	s_waitcnt lgkmcnt(0)
	v_mfma_f32_32x32x16_bf16 v[108:123], v[204:207], v[16:19], v[108:123]
	s_nop 11
	s_nop 2
	v_cvt_pk_bf16_f32 v216, v108, v109
	v_cvt_pk_bf16_f32 v217, v110, v111
	v_cvt_pk_bf16_f32 v218, v112, v113
	v_cvt_pk_bf16_f32 v219, v114, v115
	v_cvt_pk_bf16_f32 v220, v116, v117
	v_cvt_pk_bf16_f32 v221, v118, v119
	v_cvt_pk_bf16_f32 v222, v120, v121
	v_cvt_pk_bf16_f32 v223, v122, v123
	ds_write_b128 v82, v[216:219] offset:20480
	ds_write_b128 v82, v[220:223] offset:21504
	v_mbcnt_lo_u32_b32 v224, -1, 0
	v_mbcnt_hi_u32_b32 v193, -1, v224
	v_mov_b32_e32 v194, v193
	s_waitcnt vmcnt(4) lgkmcnt(0)
	s_barrier
	ds_read_b128 v[176:179], v81 offset:20480
	ds_read_b128 v[180:183], v81 offset:21504
	ds_read_b128 v[184:187], v81 offset:22528
	ds_read_b128 v[188:191], v81 offset:23552
	s_movk_i32 s7, 0x80
	s_movk_i32 s6, 0xc0
	s_mov_b32 s5, 0x10000
	s_waitcnt lgkmcnt(0)
	s_barrier
	s_cmpk_gt_u32 s3, 0xff
	s_nop 0
	v_and_b32_e32 v196, 31, v194
	v_ashrrev_i32_e32 v197, 5, v194
	v_lshlrev_b32_e32 v195, 2, v194
	v_bfe_u32 v198, v194, 2, 2
	s_cbranch_scc0 .LBB1_16
	v_lshl_add_u32 v0, s20, 2, v197
	v_lshlrev_b32_e32 v3, 2, v197
	v_add_u32_e32 v1, 2, v0
	v_lshlrev_b32_e32 v2, 9, v0
	v_and_b32_e32 v3, 12, v3
	v_bfe_u32 v0, v0, 2, 2
	v_bitop3_b32 v0, v0, v196, v3 bitop3:0x36
	v_lshl_or_b32 v199, v0, 4, v2
	v_lshlrev_b32_e32 v0, 2, v1
	s_bfe_u32 s18, s3, 0x10006
	v_and_b32_e32 v0, 12, v0
	v_bfe_u32 v2, v1, 2, 2
	v_bitop3_b32 v0, v0, v196, v2 bitop3:0x36
	v_lshrrev_b32_e32 v2, 3, v194
	s_lshl_b32 s16, s18, 8
	v_and_b32_e32 v2, 2, v2
	v_bfe_u32 v3, v194, 1, 1
	s_add_i32 s16, s16, 0
	v_lshlrev_b32_e32 v4, 3, v194
	v_lshl_add_u32 v5, v197, 11, s16
	v_bitop3_b32 v2, v2, v197, v3 bitop3:0x36
	v_and_or_b32 v4, v4, 8, v5
	v_lshlrev_b32_e32 v2, 4, v2
	v_lshlrev_b32_e32 v3, 6, v198
	v_lshl_add_u32 v4, v198, 9, v4
	v_or_b32_e32 v5, v2, v3
	v_add_u32_e32 v200, v4, v5
	v_bitop3_b32 v5, v2, v3, 32 bitop3:0xde
	v_add_u32_e32 v6, 0x1000, v4
	v_add_u32_e32 v201, v6, v5
	v_xor_b32_e32 v5, 64, v3
	v_bitop3_b32 v5, v2, v5, 32 bitop3:0xde
	v_add_u32_e32 v203, v6, v5
	v_xor_b32_e32 v5, 0x80, v3
	v_bitop3_b32 v7, v2, v3, 64 bitop3:0xf6
	v_bitop3_b32 v5, v2, v5, 32 bitop3:0xde
	v_add_u32_e32 v202, v4, v7
	v_bitop3_b32 v7, v2, v3, s7 bitop3:0xf6
	v_add_u32_e32 v205, v6, v5
	v_xor_b32_e32 v5, 0xc0, v3
	v_bitop3_b32 v3, v2, v3, s6 bitop3:0xf6
	s_and_b32 s6, s22, 2
	v_lshlrev_b32_e32 v1, 9, v1
	s_lshl_b32 s27, s6, 2
	s_lshl_b32 s7, s6, 8
	s_lshl_b32 s6, s6, 12
	v_lshl_or_b32 v208, v0, 4, v1
	s_lshl_b32 s19, s20, 11
	s_add_i32 s7, s7, 0
	s_add_i32 s6, s6, 0
	v_mov_b32_e32 v0, 0
	v_bitop3_b32 v2, v2, v5, 32 bitop3:0xde
	s_waitcnt vmcnt(0)
	s_add_i32 s19, s19, 0
	s_add_i32 s16, s7, 0x20000
	s_add_i32 s7, s7, 0x20100
	v_lshlrev_b32_e32 v209, 4, v194
	s_add_i32 s6, s6, 0x18000
	v_mov_b32_e32 v14, v0
	v_mov_b32_e32 v15, v0
	v_add_u32_e32 v204, v4, v7
	v_add_u32_e32 v206, v4, v3
	v_add_u32_e32 v207, v6, v2
	v_add_u32_e32 v212, s6, v209
	s_add_u32 s6, s8, 0xfff90000
	v_mov_b32_e32 v1, v0
	v_mov_b32_e32 v2, v0
	v_mov_b32_e32 v3, v0
	v_mov_b32_e32 v4, v0
	v_mov_b32_e32 v5, v0
	v_mov_b32_e32 v6, v0
	v_mov_b32_e32 v7, v0
	v_mov_b32_e32 v8, v0
	v_mov_b32_e32 v9, v0
	v_mov_b32_e32 v10, v0
	v_mov_b32_e32 v11, v0
	v_mov_b32_e32 v12, v0
	v_mov_b32_e32 v13, v0
	v_mov_b64_e32 v[62:63], v[14:15]
	v_mov_b64_e32 v[94:95], v[14:15]
	v_mov_b64_e32 v[126:127], v[14:15]
	v_mov_b64_e32 v[30:31], v[14:15]
	v_mov_b64_e32 v[46:47], v[14:15]
	v_mov_b64_e32 v[78:79], v[14:15]
	v_mov_b64_e32 v[110:111], v[14:15]
	v_add_u32_e32 v210, s16, v195
	v_add_u32_e32 v211, s7, v195
	s_addc_u32 s7, s9, -1
	s_mov_b32 s33, 1
	s_mov_b32 s31, 0x8000
	s_mov_b32 s29, 0x10000
	v_mov_b64_e32 v[60:61], v[12:13]
	v_mov_b64_e32 v[58:59], v[10:11]
	v_mov_b64_e32 v[56:57], v[8:9]
	v_mov_b64_e32 v[54:55], v[6:7]
	v_mov_b64_e32 v[52:53], v[4:5]
	v_mov_b64_e32 v[50:51], v[2:3]
	v_mov_b64_e32 v[48:49], v[0:1]
	v_mov_b64_e32 v[92:93], v[12:13]
	v_mov_b64_e32 v[90:91], v[10:11]
	v_mov_b64_e32 v[88:89], v[8:9]
	v_mov_b64_e32 v[86:87], v[6:7]
	v_mov_b64_e32 v[84:85], v[4:5]
	v_mov_b64_e32 v[82:83], v[2:3]
	v_mov_b64_e32 v[80:81], v[0:1]
	v_mov_b64_e32 v[124:125], v[12:13]
	v_mov_b64_e32 v[122:123], v[10:11]
	v_mov_b64_e32 v[120:121], v[8:9]
	v_mov_b64_e32 v[118:119], v[6:7]
	v_mov_b64_e32 v[116:117], v[4:5]
	v_mov_b64_e32 v[114:115], v[2:3]
	v_mov_b64_e32 v[112:113], v[0:1]
	v_mov_b64_e32 v[28:29], v[12:13]
	v_mov_b64_e32 v[26:27], v[10:11]
	v_mov_b64_e32 v[24:25], v[8:9]
	v_mov_b64_e32 v[22:23], v[6:7]
	v_mov_b64_e32 v[20:21], v[4:5]
	v_mov_b64_e32 v[18:19], v[2:3]
	v_mov_b64_e32 v[16:17], v[0:1]
	v_mov_b64_e32 v[44:45], v[12:13]
	v_mov_b64_e32 v[42:43], v[10:11]
	v_mov_b64_e32 v[40:41], v[8:9]
	v_mov_b64_e32 v[38:39], v[6:7]
	v_mov_b64_e32 v[36:37], v[4:5]
	v_mov_b64_e32 v[34:35], v[2:3]
	v_mov_b64_e32 v[32:33], v[0:1]
	v_mov_b64_e32 v[76:77], v[12:13]
	v_mov_b64_e32 v[74:75], v[10:11]
	v_mov_b64_e32 v[72:73], v[8:9]
	v_mov_b64_e32 v[70:71], v[6:7]
	v_mov_b64_e32 v[68:69], v[4:5]
	v_mov_b64_e32 v[66:67], v[2:3]
	v_mov_b64_e32 v[64:65], v[0:1]
	v_mov_b64_e32 v[108:109], v[12:13]
	v_mov_b64_e32 v[106:107], v[10:11]
	v_mov_b64_e32 v[104:105], v[8:9]
	v_mov_b64_e32 v[102:103], v[6:7]
	v_mov_b64_e32 v[100:101], v[4:5]
	v_mov_b64_e32 v[98:99], v[2:3]
	v_mov_b64_e32 v[96:97], v[0:1]
	s_waitcnt lgkmcnt(0)
	s_barrier
